# down-queue LAG 19 instead of 15 (gate_up stays 15), on top of the hand-written prefix tables
# baseline (speedup 1.0000x reference)
; #define LAS3 __attribute__((address_space(3)))
; __device__ __forceinline__ int lane_id() { int r; asm volatile("v_mbcnt_lo_u32_b32 %0, -1, 0\n\tv_mbcnt_hi_u32_b32 %0, -1, %0" : "=v"(r)); return r; }
; template <int EPI>
; __device__ __forceinline__ int* moe_phase(const Params& p, LAS3 char* lds, int wid, int* pend_in) {
;     ...
;     { const int t0 = wid * 64 + lane_id();
;       if (t0 < 8) { int a = 0; LAS3 int* pq = pre + t0 * 128;
;           for (int s = 0; s <= NSL; ++s) { pq[s] = a;
;               if (s < NSL) { int nv = (s < NS && mtv[t0 + 8 * (s / NCOL)] > 0) ? 1 : 0; const int sc = s - MOE_LAG;
;                   if (EPI == 2 && s < MOE_LAG3 && mtv[t0 + 8 * (s >> 3)] > 0) nv += 1;
;                   if (sc >= 0 && sc < NS) nv += mtv[t0 + 8 * (sc / NCOL)];
;                   a += nv; } } } }
.LBB0_514:
	s_or_b64 exec, exec, s[0:1]
	v_mbcnt_lo_u32_b32 v0, -1, 0
	v_mbcnt_hi_u32_b32 v0, -1, v0
	s_nop 0
	v_add_u32_e32 v0, s75, v0
	v_cmp_gt_i32_e32 vcc, 8, v0
	s_and_saveexec_b64 s[0:1], vcc
	s_cbranch_execz .LBB0_516
	s_waitcnt vmcnt(0)
	v_lshl_add_u32 v1, v0, 9, 0
	v_add_u32_e32 v1, 0x22000, v1
	v_lshl_add_u32 v3, v0, 2, 0
	v_add_u32_e32 v3, 0x21300, v3
	ds_read_b32 v4, v3
	ds_read_b32 v5, v3 offset:32
	ds_read_b32 v6, v3 offset:64
	ds_read_b32 v7, v3 offset:96
	v_mov_b32_e32 v2, 0
	s_waitcnt lgkmcnt(0)
	v_cmp_lt_i32_e32 vcc, 0, v4
	s_nop 1
	v_cndmask_b32_e64 v3, 0, 1, vcc
	ds_write_b32 v1, v2
	v_add_u32_e32 v2, v2, v3
	ds_write_b32 v1, v2 offset:4
	v_add_u32_e32 v2, v2, v3
	ds_write_b32 v1, v2 offset:8
	v_add_u32_e32 v2, v2, v3
	ds_write_b32 v1, v2 offset:12
	v_add_u32_e32 v2, v2, v3
	ds_write_b32 v1, v2 offset:16
	v_add_u32_e32 v2, v2, v3
	ds_write_b32 v1, v2 offset:20
	v_add_u32_e32 v2, v2, v3
	ds_write_b32 v1, v2 offset:24
	v_add_u32_e32 v2, v2, v3
	ds_write_b32 v1, v2 offset:28
	v_add_u32_e32 v2, v2, v3
	v_cmp_lt_i32_e32 vcc, 0, v5
	s_nop 1
	v_cndmask_b32_e64 v3, 0, 1, vcc
	ds_write_b32 v1, v2 offset:32
	v_add_u32_e32 v2, v2, v3
	ds_write_b32 v1, v2 offset:36
	v_add_u32_e32 v2, v2, v3
	ds_write_b32 v1, v2 offset:40
	v_add_u32_e32 v2, v2, v3
	ds_write_b32 v1, v2 offset:44
	v_add_u32_e32 v2, v2, v3
	ds_write_b32 v1, v2 offset:48
	v_add_u32_e32 v2, v2, v3
	ds_write_b32 v1, v2 offset:52
	v_add_u32_e32 v2, v2, v3
	ds_write_b32 v1, v2 offset:56
	v_add_u32_e32 v2, v2, v3
	ds_write_b32 v1, v2 offset:60
	v_add_u32_e32 v2, v2, v3
	v_cmp_lt_i32_e32 vcc, 0, v6
	s_nop 1
	v_cndmask_b32_e64 v3, 0, 1, vcc
	ds_write_b32 v1, v2 offset:64
	v_add_u32_e32 v2, v2, v3
	ds_write_b32 v1, v2 offset:68
	v_add_u32_e32 v2, v2, v3
	ds_write_b32 v1, v2 offset:72
	v_add_u32_e32 v2, v2, v3
	v_cmp_lt_i32_e32 vcc, 0, v6
	s_nop 1
	v_addc_co_u32_e32 v3, vcc, 0, v4, vcc
	ds_write_b32 v1, v2 offset:76
	v_add_u32_e32 v2, v2, v3
	ds_write_b32 v1, v2 offset:80
	v_add_u32_e32 v2, v2, v3
	ds_write_b32 v1, v2 offset:84
	v_add_u32_e32 v2, v2, v3
	ds_write_b32 v1, v2 offset:88
	v_add_u32_e32 v2, v2, v3
	ds_write_b32 v1, v2 offset:92
	v_add_u32_e32 v2, v2, v3
	v_cmp_lt_i32_e32 vcc, 0, v7
	s_nop 1
	v_addc_co_u32_e32 v3, vcc, 0, v4, vcc
	ds_write_b32 v1, v2 offset:96
	v_add_u32_e32 v2, v2, v3
	ds_write_b32 v1, v2 offset:100
	v_add_u32_e32 v2, v2, v3
	ds_write_b32 v1, v2 offset:104
	v_add_u32_e32 v2, v2, v3
	v_cmp_lt_i32_e32 vcc, 0, v7
	s_nop 1
	v_addc_co_u32_e32 v3, vcc, 0, v5, vcc
	ds_write_b32 v1, v2 offset:108
	v_add_u32_e32 v2, v2, v3
	ds_write_b32 v1, v2 offset:112
	v_add_u32_e32 v2, v2, v3
	ds_write_b32 v1, v2 offset:116
	v_add_u32_e32 v2, v2, v3
	ds_write_b32 v1, v2 offset:120
	v_add_u32_e32 v2, v2, v3
	ds_write_b32 v1, v2 offset:124
	v_add_u32_e32 v2, v2, v3
	v_mov_b32_e32 v3, v5
	ds_write_b32 v1, v2 offset:128
	v_add_u32_e32 v2, v2, v3
	ds_write_b32 v1, v2 offset:132
	v_add_u32_e32 v2, v2, v3
	ds_write_b32 v1, v2 offset:136
	v_add_u32_e32 v2, v2, v3
	v_mov_b32_e32 v3, v6
	ds_write_b32 v1, v2 offset:140
	v_add_u32_e32 v2, v2, v3
	ds_write_b32 v1, v2 offset:144
	v_add_u32_e32 v2, v2, v3
	ds_write_b32 v1, v2 offset:148
	v_add_u32_e32 v2, v2, v3
	ds_write_b32 v1, v2 offset:152
	v_add_u32_e32 v2, v2, v3
	ds_write_b32 v1, v2 offset:156
	v_add_u32_e32 v2, v2, v3
	ds_write_b32 v1, v2 offset:160
	v_add_u32_e32 v2, v2, v3
	ds_write_b32 v1, v2 offset:164
	v_add_u32_e32 v2, v2, v3
	ds_write_b32 v1, v2 offset:168
	v_add_u32_e32 v2, v2, v3
	v_mov_b32_e32 v3, v7
	ds_write_b32 v1, v2 offset:172
	v_add_u32_e32 v2, v2, v3
	ds_write_b32 v1, v2 offset:176
	v_add_u32_e32 v2, v2, v3
	ds_write_b32 v1, v2 offset:180
	v_add_u32_e32 v2, v2, v3
	ds_write_b32 v1, v2 offset:184
	v_add_u32_e32 v2, v2, v3
	ds_write_b32 v1, v2 offset:188
	v_add_u32_e32 v2, v2, v3
	ds_write_b32 v1, v2 offset:192
	v_add_u32_e32 v2, v2, v3
	ds_write_b32 v1, v2 offset:196
	v_add_u32_e32 v2, v2, v3
	ds_write_b32 v1, v2 offset:200
	v_add_u32_e32 v2, v2, v3
	ds_write_b32 v1, v2 offset:204

; #define LAS3 __attribute__((address_space(3)))
; __device__ __forceinline__ int lane_id() { int r; asm volatile("v_mbcnt_lo_u32_b32 %0, -1, 0\n\tv_mbcnt_hi_u32_b32 %0, -1, %0" : "=v"(r)); return r; }
; #define LD_WAIT(r) asm volatile("s_waitcnt vmcnt(0)" : "+v"(r) :: "memory")
; template <int EPI>
; __device__ __forceinline__ int* moe_phase(const Params& p, LAS3 char* lds, int wid, int* pend_in) {
;     ...
;         __syncthreads();
;         const unsigned code = (unsigned)__builtin_amdgcn_readfirstlane((int)slot[par]);
;         if (code == 0xFFFFFFFFu) break;
;         const int qq = (int)(code >> 20), i = (int)(code & 0xFFFFFu);
;         bool ran = false;
;         LAS3 int* pq = pre + qq * 128;
;         const int total = __builtin_amdgcn_readfirstlane(pq[NSL]);
;     ...
;             const int t0 = wid * 64 + lane_id();
;             if (t0 == 0) { unsigned cv[8];
;                 unsigned qx; asm volatile("s_getreg_b32 %0, hwreg(HW_REG_XCC_ID, 0, 3)" : "=s"(qx));
; #pragma unroll
;                 for (int d = 0; d < 8; ++d) cv[d] = (unsigned)ld_early((const int*)&qctr[(qx + d) & 7u]);
; #pragma unroll
;                 for (int d = 0; d < 8; ++d) LD_WAIT(cv[d]);
;                 unsigned c = 0xFFFFFFFFu;
; #pragma unroll
;                 for (int d = 7; d >= 0; --d) if (cv[d] < (unsigned)pre[((qx + d) & 7u) * 128 + NSL]) c = (qx + d) & 7u;
;                 if (c != 0xFFFFFFFFu) { const unsigned cq = (unsigned)__builtin_amdgcn_readfirstlane((int)c); unsigned c0 = inc_early(&qctr[cq]); LD_WAIT(c0); c = (cq << 20) | c0; }
;                 slot[par ^ 1] = c; }
.LBB0_522:
	s_lshl_b32 s0, s10, 2
	s_add_i32 s0, s0, 0
	s_add_i32 s0, s0, 0x21040
	v_mov_b32_e32 v0, s0
	s_waitcnt lgkmcnt(0)
	s_barrier
	ds_read_b32 v0, v0
	s_mov_b64 s[0:1], -1
	s_waitcnt lgkmcnt(0)
	v_readfirstlane_b32 s25, v0
	s_cmp_eq_u32 s25, -1
	s_cbranch_scc1 .LBB0_521
	s_lshr_b32 s19, s25, 20
	s_lshl_b32 s0, s19, 9
	s_add_i32 s14, s0, 0
	s_add_i32 s14, s14, 0x22000
	v_mov_b32_e32 v0, s14
	ds_read_b32 v0, v0 offset:204
	s_and_b32 s15, s25, 0xfffff
	s_waitcnt lgkmcnt(0)
	v_readfirstlane_b32 s0, v0
	s_cmp_ge_i32 s15, s0
	s_mov_b64 s[0:1], -1
	s_cbranch_scc0 .LBB0_529
	v_mbcnt_lo_u32_b32 v0, -1, 0
	v_mbcnt_hi_u32_b32 v0, -1, v0
	s_nop 0
	v_sub_u32_e32 v0, 0, v0
	v_cmp_eq_u32_e32 vcc, s75, v0
	s_and_saveexec_b64 s[0:1], vcc
	s_cbranch_execz .LBB0_528
	s_getreg_b32 s30, hwreg(HW_REG_XCC_ID, 0, 3)
	s_and_b32 s4, s30, 7
	s_lshl_b32 s26, s4, 2
	s_add_u32 s26, s2, s26
	s_addc_u32 s27, s3, 0
	v_mov_b32 v0, 0
	s_nop 4
	global_load_dword v1, v0, s[26:27] sc1
	s_add_i32 s26, s30, 1
	s_and_b32 s26, s26, 7
	s_lshl_b32 s27, s26, 2
	s_add_u32 s28, s2, s27
	s_addc_u32 s29, s3, 0
	s_add_i32 s27, s30, 2
	s_and_b32 s27, s27, 7
	v_mov_b32 v0, 0
	s_nop 4
	global_load_dword v2, v0, s[28:29] sc1
	s_lshl_b32 s28, s27, 2
	s_add_u32 s28, s2, s28
	s_addc_u32 s29, s3, 0
	v_mov_b32 v0, 0
	s_nop 4
	global_load_dword v3, v0, s[28:29] sc1
	s_add_i32 s28, s30, 3
	s_and_b32 s31, s28, 7
	s_lshl_b32 s28, s31, 2
	s_add_u32 s28, s2, s28
	s_addc_u32 s29, s3, 0
	s_xor_b32 s34, s4, 4
	s_waitcnt vmcnt(14)
	v_mov_b32 v0, 0
	s_nop 4
	global_load_dword v4, v0, s[28:29] sc1
	s_lshl_b32 s28, s34, 2
	s_add_u32 s28, s2, s28
	s_addc_u32 s29, s3, 0
	v_mov_b32 v0, 0
	s_nop 4
	global_load_dword v5, v0, s[28:29] sc1
	s_add_i32 s28, s30, 5
	s_and_b32 s35, s28, 7
	s_lshl_b32 s28, s35, 2
	s_add_u32 s28, s2, s28
	s_addc_u32 s29, s3, 0
	v_mov_b32 v0, 0
	s_nop 4
	global_load_dword v6, v0, s[28:29] sc1
	s_add_i32 s28, s30, 6
	s_and_b32 s36, s28, 7
	s_lshl_b32 s28, s36, 2
	s_add_u32 s28, s2, s28
	s_addc_u32 s29, s3, 0
	s_add_i32 s30, s30, -1
	s_and_b32 s30, s30, 7
	v_mov_b32 v0, 0
	s_nop 4
	global_load_dword v7, v0, s[28:29] sc1
	s_lshl_b32 s28, s30, 2
	s_add_u32 s28, s2, s28
	s_addc_u32 s29, s3, 0
	s_waitcnt vmcnt(13)
	v_mov_b32 v0, 0
	s_nop 4
	global_load_dword v8, v0, s[28:29] sc1
	s_waitcnt vmcnt(0)
	s_waitcnt vmcnt(0)
	s_waitcnt vmcnt(0)
	s_waitcnt vmcnt(0)
	s_waitcnt vmcnt(0)
	s_waitcnt vmcnt(0)
	s_lshl_b32 s28, s30, 9
	s_add_i32 s29, 0, 0x22000
	s_waitcnt vmcnt(0)
	s_add_i32 s28, s29, s28
	s_waitcnt vmcnt(0)
	v_mov_b32_e32 v0, s28
	ds_read_b32 v0, v0 offset:204
	s_lshl_b32 s28, s36, 9
	s_add_i32 s28, s29, s28
	s_waitcnt lgkmcnt(0)
	v_cmp_lt_u32_e32 vcc, v8, v0
	v_mov_b32_e32 v8, s28
	ds_read_b32 v8, v8 offset:204
	v_mov_b32_e32 v0, s30
	s_lshl_b32 s28, s35, 9
	v_cndmask_b32_e32 v0, -1, v0, vcc
	s_add_i32 s28, s29, s28
	s_waitcnt lgkmcnt(0)
	v_cmp_lt_u32_e32 vcc, v7, v8
	v_mov_b32_e32 v7, s36
	s_nop 0
	v_cndmask_b32_e32 v0, v0, v7, vcc
	v_mov_b32_e32 v7, s28
	ds_read_b32 v7, v7 offset:204
	s_lshl_b32 s28, s34, 9
	s_add_i32 s28, s29, s28
	s_waitcnt lgkmcnt(0)
	v_cmp_lt_u32_e32 vcc, v6, v7
	v_mov_b32_e32 v6, s35
	s_nop 0
	v_cndmask_b32_e32 v0, v0, v6, vcc
	v_mov_b32_e32 v6, s28
	ds_read_b32 v6, v6 offset:204
	s_lshl_b32 s28, s31, 9
	s_add_i32 s28, s29, s28
	s_waitcnt lgkmcnt(0)
	v_cmp_lt_u32_e32 vcc, v5, v6
	v_mov_b32_e32 v5, s34
	s_nop 0
	v_cndmask_b32_e32 v0, v0, v5, vcc
	v_mov_b32_e32 v5, s28
	ds_read_b32 v5, v5 offset:204
	s_lshl_b32 s28, s27, 9
	s_add_i32 s28, s29, s28
	s_waitcnt lgkmcnt(0)
	v_cmp_lt_u32_e32 vcc, v4, v5
	v_mov_b32_e32 v4, s31
	s_nop 0
	v_cndmask_b32_e32 v0, v0, v4, vcc
	v_mov_b32_e32 v4, s28
	ds_read_b32 v4, v4 offset:204
	s_waitcnt lgkmcnt(0)
	v_cmp_lt_u32_e32 vcc, v3, v4
	v_mov_b32_e32 v3, s27
	s_lshl_b32 s27, s26, 9
	s_add_i32 s27, s29, s27
	v_cndmask_b32_e32 v0, v0, v3, vcc
	v_mov_b32_e32 v3, s27
	ds_read_b32 v3, v3 offset:204
	s_waitcnt lgkmcnt(0)
	v_cmp_lt_u32_e32 vcc, v2, v3
	v_mov_b32_e32 v2, s26
	s_lshl_b32 s26, s4, 9
	s_add_i32 s26, s29, s26
	v_cndmask_b32_e32 v0, v0, v2, vcc
	v_mov_b32_e32 v2, s26
	ds_read_b32 v2, v2 offset:204
	s_waitcnt lgkmcnt(0)
	v_cmp_lt_u32_e32 vcc, v1, v2
	v_mov_b32_e32 v1, s4
	s_nop 0
	v_cndmask_b32_e32 v1, v0, v1, vcc
	v_cmp_ne_u32_e32 vcc, -1, v1
	v_mov_b32_e32 v0, -1
	s_and_saveexec_b64 s[26:27], vcc
	s_cbranch_execz .LBB0_527
	v_readfirstlane_b32 s4, v1
	s_lshl_b64 s[28:29], s[4:5], 2
	s_add_u32 s28, s2, s28
	s_addc_u32 s29, s3, s29
	v_mov_b32 v0, 0
	v_mov_b32 v1, 1
	s_nop 4
	global_atomic_add v1, v0, v1, s[28:29] sc0
	s_nop 0
	s_waitcnt vmcnt(0)
	s_nop 0
	v_lshl_or_b32 v0, s4, 20, v1

; __device__ __forceinline__ int lane_id() { int r; asm volatile("v_mbcnt_lo_u32_b32 %0, -1, 0\n\tv_mbcnt_hi_u32_b32 %0, -1, %0" : "=v"(r)); return r; }
; template <int EPI>
; __device__ __forceinline__ int* moe_phase(const Params& p, LAS3 char* lds, int wid, int* pend_in) {
;     ...
;         if (i < total) {
;             int s, j;
;             { const int l = lane_id();
;               const bool c1 = (l + 1 <= NSL) && (pq[(l + 1 <= NSL) ? l + 1 : 0] <= i), c2 = (l + 65 <= NSL) && (pq[(l + 65 <= NSL) ? l + 65 : 0] <= i);
;               s = __builtin_popcountll(__builtin_amdgcn_ballot_w64(c1)) + __builtin_popcountll(__builtin_amdgcn_ballot_w64(c2));
;               j = i - __builtin_amdgcn_readfirstlane(pq[s]); }
.LBB0_529:
	s_andn2_b64 vcc, exec, s[0:1]
	s_cbranch_vccnz .LBB0_520
	v_mbcnt_lo_u32_b32 v1, -1, 0
	v_mbcnt_hi_u32_b32 v1, -1, v1
	s_mov_b64 s[0:1], 0
	v_cmp_gt_i32_e32 vcc, 51, v1
	v_lshl_add_u32 v0, v1, 2, s14
	s_mov_b64 s[26:27], 0
	s_and_saveexec_b64 s[28:29], vcc
	s_cbranch_execz .LBB0_532
	ds_read_b32 v2, v0 offset:4
	s_waitcnt lgkmcnt(0)
	v_cmp_ge_i32_e32 vcc, s15, v2
	s_and_b64 s[26:27], vcc, exec
.LBB0_532:
	s_or_b64 exec, exec, s[28:29]
	s_movk_i32 s4, 0xfff3
	v_cmp_gt_i32_e32 vcc, s4, v1
	s_and_saveexec_b64 s[28:29], vcc
	s_cbranch_execz .LBB0_534
	ds_read_b32 v0, v0 offset:260
	s_waitcnt lgkmcnt(0)
	v_cmp_ge_i32_e32 vcc, s15, v0
	s_and_b64 s[0:1], vcc, exec

; template <int EPI>
; __device__ __forceinline__ int* moe_phase(const Params& p, LAS3 char* lds, int wid, int* pend_in) {
;     ...
;             const bool hasP = (s < NS) && (__builtin_amdgcn_readfirstlane(mtv[qq + 8 * ((s < NS) ? s / NCOL : 0)]) > 0);
;             const bool conv = hasP && j == 0;
;             const bool hasX = (EPI == 2) && (s < MOE_LAG3) && (__builtin_amdgcn_readfirstlane(mtv[qq + 8 * ((s < MOE_LAG3) ? (s >> 3) : 0)]) > 0);
;             const bool xconv = hasX && j == (hasP ? 1 : 0);
;             const int k = conv ? 0 : j - (hasP ? 1 : 0) - (hasX ? 1 : 0);
;             const int sl = conv ? s : s - MOE_LAG;
.LBB0_536:
	s_cmp_eq_u32 s15, s34
	s_cselect_b64 s[0:1], -1, 0
	s_and_b64 s[0:1], s[30:31], s[0:1]
	s_add_i32 s14, s4, -19
	s_and_b64 s[28:29], s[0:1], exec
	s_cselect_b32 s14, s4, s14
	s_cmp_gt_u32 s14, 31
	s_cselect_b64 s[28:29], -1, 0
	s_and_b64 vcc, exec, s[28:29]
	s_cbranch_vccz .LBB0_539
	s_andn2_b64 vcc, exec, s[28:29]
	s_cbranch_vccz .LBB0_540
